# MoE unit scheduling: expert lookup by one lane-indexed LDS read + v_cmp + s_bcnt1 + v_readlane instead of a 15-step compare/add chain with three LDS round trips
# baseline (speedup 1.0000x reference)
.LBB0_1053:
	s_mul_hi_i32 s4, s19, 0x2aaaaaab
	s_lshr_b32 s5, s4, 31
	s_add_i32 s24, s4, s5
	s_mul_i32 s4, s24, -6
	s_add_i32 s22, s4, s19
	v_mbcnt_lo_u32_b32 v4, -1, 0
	v_mbcnt_hi_u32_b32 v4, -1, v4
	v_lshlrev_b32_e32 v4, 2, v4
	ds_read_b32 v5, v4 offset:64
	s_waitcnt lgkmcnt(0)
	v_cmp_ge_i32_e64 s[4:5], s24, v5
	s_nop 1
	s_and_b32 s4, s4, 0xfffe
	s_bcnt1_i32_b32 s4, s4
	s_nop 3
	v_readlane_b32 s5, v5, s4
	v_mov_b32_e32 v198, s4
	s_nop 0
	s_sub_i32 s5, s24, s5
	v_mov_b32_e32 v199, s5

.LBB0_1104:
	s_ashr_i32 s0, s4, 31
	s_lshr_b32 s0, s0, 30
	s_add_i32 s0, s4, s0
	s_ashr_i32 s3, s0, 2
	s_and_b32 s0, s0, -4
	s_sub_i32 s72, s4, s0
	s_mov_b32 s0, 48
	v_mbcnt_lo_u32_b32 v2, -1, 0
	v_mbcnt_hi_u32_b32 v2, -1, v2
	v_lshlrev_b32_e32 v2, 2, v2
	ds_read_b32 v3, v2 offset:64
	s_waitcnt lgkmcnt(0)
	v_cmp_ge_i32_e64 s[4:5], s3, v3
	s_nop 1
	s_and_b32 s4, s4, 0xfffe
	s_bcnt1_i32_b32 s4, s4
	s_nop 3
	v_readlane_b32 s5, v3, s4
	v_mov_b32_e32 v218, s4
	s_nop 0
	s_sub_i32 s5, s3, s5
	v_mov_b32_e32 v219, s5
